# plus: P10 expert-weight (B tile) LDS-DMA loads non-temporal
# baseline (speedup 1.0000x reference)
; #define PG8_STAGE(bufoff, gbase, voff) do { _Pragma("unroll") for (int _i = 0; _i < 2; ++_i) \
;         __builtin_amdgcn_global_load_lds((const unsigned*)((const char*)(gbase) + (voff)[_i]), (PG8_LAS unsigned*)(lds + (bufoff) + ldsw + _i * 8192), 16, 0, 0); } while (0)
; #define PG8_WAIT_V(n) asm volatile("s_waitcnt vmcnt(" #n ")" ::: "memory")
; #define PG8_BAR __builtin_amdgcn_s_barrier()
; #define PG8_STAGE(bufoff, gbase, voff) do { _Pragma("unroll") for (int _i = 0; _i < 2; ++_i) \
;         __builtin_amdgcn_global_load_lds((const unsigned*)((const char*)(gbase) + (voff)[_i]), (PG8_LAS unsigned*)(lds + (bufoff) + ldsw + _i * 8192), 16, 0, 0); } while (0)
; #define PG8_WAIT_V(n) asm volatile("s_waitcnt vmcnt(" #n ")" ::: "memory")
; #define PG8_BAR __builtin_amdgcn_s_barrier()
;     __device__ __forceinline__ bool next(int i, pg8::Unit& u) const { const int s = i >= R ? 1 : 0; const bool ok = so.next(i - s * R, u); u.sel = s; return ok && i < 2 * R; }
; template <class Epi, class Sched>
; __device__ __forceinline__ void gemm_phase_gather(PG8_LAS unsigned char* lds, const Gemm g, const int* __restrict__ gidx, PG8_LAS int* itab  , const Sched& S, const Epi& E) {
;     ...
;     const char* cB = (const char*)g.Bt + (size_t)cur.pn * tstep;
;     S.a_ready(cur);
;     PG8_STAGE(PG8_SB(0, 0), cB, voffB); PG8_STAGE(PG8_SB(0, 1), cB + hstep, voffB); PG8_STAGE(PG8_SA(0, 0), gA, cvo[0]); PG8_STAGE(PG8_SA(0, 1), gA, cvo[1]);
;     if (wr == 1) PG8_BAR;
;     PG8_WAIT_V(2); PG8_BAR;
;     PG8_STAGE(PG8_SB(1, 0), cB + kstep, voffB); PG8_STAGE(PG8_SA(1, 0), gA + kstep, cvo[0]); PG8_STAGE(PG8_SB(1, 1), cB + hstep + kstep, voffB);
;     PG8_WAIT_V(6); PG8_BAR;
;     for (;;) {
;         const bool has_next = S.next(ui + 1, nxt);
.LBB0_1270:
	s_lshl_b32 s11, s11, 3
	s_sub_i32 s10, s10, s11
	s_sext_i32_i8 s10, s10
	s_and_b32 s11, s10, 1
	s_lshl_b32 s10, s10, 3
	s_and_b32 s10, s10, 0x7ffffff0
	s_add_i32 s10, s10, s9
	s_lshl_b32 s8, s8, 5
	s_lshl_b32 s9, s10, 1
	s_and_b32 s17, s8, 0x60
	s_or_b32 s45, s9, s11
	s_lshl_b32 s16, s7, 13
	s_lshl_b32 s18, s17, 7
	s_add_u32 s8, s0, 0x2800000
	s_mov_b64 s[10:11], 0x80
	s_addc_u32 s9, s1, 0
	s_add_i32 m0, s21, 0x18000
	v_lshl_add_u64 v[4:5], v[4:5], 0, s[10:11]
	s_waitcnt vmcnt(2)
	s_barrier
	global_load_lds_dwordx4 v[4:5], off nt
	s_add_i32 m0, s21, 0x1a000
	s_add_u32 s12, s0, 0xe800080
	v_lshl_add_u64 v[2:3], v[2:3], 0, s[10:11]
	s_addc_u32 s13, s1, 0
	s_add_i32 s35, s21, 0x8000
	s_add_i32 s36, s21, 0xa000
	global_load_lds_dwordx4 v[2:3], off nt
	v_lshl_add_u64 v[2:3], s[12:13], 0, v[134:135]
	s_mov_b32 m0, s35
	s_add_u32 s14, s22, 0x80080
	global_load_lds_dwordx4 v[2:3], off nt
	v_lshl_add_u64 v[2:3], s[12:13], 0, v[140:141]
	s_mov_b32 m0, s36
	s_addc_u32 s15, s23, 0
	global_load_lds_dwordx4 v[2:3], off nt
	s_add_i32 m0, s21, 0x1c000
	v_lshl_add_u64 v[2:3], s[14:15], 0, v[130:131]
	global_load_lds_dwordx4 v[2:3], off nt
	v_lshl_add_u64 v[2:3], s[14:15], 0, v[132:133]
	s_add_i32 m0, s21, 0x1e000
	v_lshlrev_b32_e32 v4, 6, v0
	global_load_lds_dwordx4 v[2:3], off nt
	v_and_b32_e32 v2, 15, v0
	v_lshl_or_b32 v141, s7, 6, v2
	v_lshlrev_b32_e32 v3, 1, v6
	s_movk_i32 s7, 0x3c0
	v_lshl_or_b32 v2, v2, 6, v3
	v_and_or_b32 v3, v4, s7, v3
	v_lshlrev_b32_e32 v4, 2, v0
	v_and_b32_e32 v4, 32, v4
	s_waitcnt vmcnt(6)
	s_cmpk_lt_u32 s6, 0x100
	v_bitop3_b32 v2, v2, s16, v4 bitop3:0xde
	v_bitop3_b32 v148, s18, v3, v4 bitop3:0xf6
	s_cselect_b64 s[14:15], -1, 0
	s_add_i32 s38, 0, 0x10000
	s_add_i32 s39, 0, 0x14000
	s_mov_b32 s37, 0
	v_or_b32_e32 v149, s17, v6
	v_add_u32_e32 v150, s38, v148
	v_add_u32_e32 v151, s39, v148
	v_add_u32_e32 v152, 0, v2
	s_mov_b32 s40, 0x80000
	s_mov_b32 s41, 0x90000
	s_mov_b32 s42, 0xa0000
	s_add_i32 s43, s21, 0xc000
	v_mov_b32_e32 v157, v134
	s_barrier
	s_branch .LBB0_1273

; #define PG8_STAGE(bufoff, gbase, voff) do { _Pragma("unroll") for (int _i = 0; _i < 2; ++_i) \
;         __builtin_amdgcn_global_load_lds((const unsigned*)((const char*)(gbase) + (voff)[_i]), (PG8_LAS unsigned*)(lds + (bufoff) + ldsw + _i * 8192), 16, 0, 0); } while (0)
; #define PG8_LDA(dst, b, h) do { _Pragma("unroll") for (int m = 0; m < 4; ++m) _Pragma("unroll") for (int k = 0; k < 2; ++k) dst[m][k] = *(const PG8_LAS bf16x8*)(lds + PG8_SA(b, h) + aoff + m * 2048 + k * 1024); } while (0)
; #define PG8_LDB(dst, b, h) do { _Pragma("unroll") for (int n = 0; n < 2; ++n) _Pragma("unroll") for (int k = 0; k < 2; ++k) dst[n][k] = *(const PG8_LAS bf16x8*)(lds + PG8_SB(b, h) + boff + n * 2048 + k * 1024); } while (0)
; #define PG8_MMA(ai, bj, At, Bt) do { __builtin_amdgcn_s_setprio(1); _Pragma("unroll") for (int m = 0; m < 4; ++m) _Pragma("unroll") for (int n = 0; n < 2; ++n) _Pragma("unroll") for (int k = 0; k < 2; ++k) \
;         acc[ai][bj][m][n] = __builtin_amdgcn_mfma_f32_16x16x32_bf16(Bt[n][k], At[m][k], acc[ai][bj][m][n], 0, 0, 0); __builtin_amdgcn_s_setprio(0); } while (0)
; #define PG8_WAIT_V(n) asm volatile("s_waitcnt vmcnt(" #n ")" ::: "memory")
; template <class Epi, class Sched>
; __device__ __forceinline__ void gemm_phase_gather(PG8_LAS unsigned char* lds, const Gemm g, const int* __restrict__ gidx, PG8_LAS int* itab  , const Sched& S, const Epi& E) {
;     ...
;             const char* a2 = last ? gA : gA + (size_t)(t + 2) * kstep; const char* b2 = last ? nB : cB + (size_t)(t + 2) * kstep;
;             const char* a3 = a2 + kstep; const char* b3 = b2 + kstep;
;             unsigned vo2[2][2];
; #pragma unroll
;             for (int _h = 0; _h < 2; ++_h)
; #pragma unroll
;                 for (int _i = 0; _i < 2; ++_i) vo2[_h][_i] = last ? nvo[_h][_i] : cvo[_h][_i];
;             if (last && has_next) S.a_ready(nxt);
;             PG8_LDB(B0, 0, 0); PG8_LDB(B1, 0, 1); PG8_SCHED; PG8_LDA(At, 0, 0); PG8_STAGE(PG8_SA(1, 1), a1, cvo[1]);
;             PG8_WAIT_V(8); PG8_WAIT_L(0); PG8_BAR; PG8_MMA(0, 0, At, B0); PG8_MMA(0, 1, At, B1); PG8_BAR; PG8_SCHED;
;             PG8_LDA(At, 0, 1); PG8_STAGE(PG8_SB(0, 0), b2, voffB); PG8_STAGE(PG8_SB(0, 1), b2 + hstep, voffB); PG8_STAGE(PG8_SA(0, 0), a2, vo2[0]);
;             PG8_WAIT_V(8); PG8_WAIT_L(0); PG8_BAR; PG8_MMA(1, 0, At, B0); PG8_MMA(1, 1, At, B1); PG8_BAR; PG8_SCHED;
.LBB0_1278:
	ds_read_b128 v[158:161], v150
	ds_read_b128 v[162:165], v150 offset:1024
	ds_read_b128 v[166:169], v150 offset:2048
	ds_read_b128 v[170:173], v150 offset:3072
	ds_read_b128 v[174:177], v151
	ds_read_b128 v[178:181], v151 offset:1024
	ds_read_b128 v[182:185], v151 offset:2048
	ds_read_b128 v[188:191], v151 offset:3072
	s_add_u32 s24, s0, s22
	s_addc_u32 s25, s1, s23
	s_add_u32 s26, s24, 0xe800100
	s_addc_u32 s27, s25, 0
	s_add_u32 s50, s47, s22
	s_addc_u32 s51, s48, s23
	s_cmpk_eq_i32 s22, 0xf00
	s_cselect_b64 vcc, -1, 0
	s_and_b64 s[24:25], vcc, exec
	v_cndmask_b32_e32 v134, v157, v153, vcc
	s_cselect_b32 s27, s3, s27
	s_cselect_b32 s26, s2, s26
	v_cndmask_b32_e32 v224, v140, v154, vcc
	v_cndmask_b32_e32 v137, v138, v155, vcc
	v_cndmask_b32_e32 v139, v136, v156, vcc
	s_cselect_b32 s25, s17, s51
	s_cselect_b32 s24, s46, s50
	s_mov_b32 m0, s43
	v_lshl_add_u64 v[226:227], v[144:145], 0, s[22:23]
	ds_read_b128 v[192:195], v152
	ds_read_b128 v[196:199], v152 offset:1024
	ds_read_b128 v[200:203], v152 offset:2048
	ds_read_b128 v[204:207], v152 offset:3072
	ds_read_b128 v[208:211], v152 offset:4096
	ds_read_b128 v[212:215], v152 offset:5120
	ds_read_b128 v[216:219], v152 offset:6144
	ds_read_b128 v[220:223], v152 offset:7168
	global_load_lds_dwordx4 v[226:227], off nt
	v_lshl_add_u64 v[226:227], v[142:143], 0, s[22:23]
	s_add_i32 m0, s21, 0xe000
	s_nop 0
	global_load_lds_dwordx4 v[226:227], off nt
	s_waitcnt vmcnt(8)
	s_waitcnt lgkmcnt(0)
	s_barrier
	s_setprio 1
	s_waitcnt lgkmcnt(0)
	v_mfma_f32_16x16x32_bf16 v[126:129], v[158:161], v[192:195], v[126:129]
	v_mfma_f32_16x16x32_bf16 v[122:125], v[166:169], v[192:195], v[122:125]
	v_mfma_f32_16x16x32_bf16 v[110:113], v[158:161], v[200:203], v[110:113]
	v_mfma_f32_16x16x32_bf16 v[106:109], v[166:169], v[200:203], v[106:109]
	v_mfma_f32_16x16x32_bf16 v[94:97], v[158:161], v[208:211], v[94:97]
	v_mfma_f32_16x16x32_bf16 v[90:93], v[166:169], v[208:211], v[90:93]
	v_mfma_f32_16x16x32_bf16 v[78:81], v[158:161], v[216:219], v[78:81]
	v_mfma_f32_16x16x32_bf16 v[74:77], v[166:169], v[216:219], v[74:77]
	v_mfma_f32_16x16x32_bf16 v[126:129], v[162:165], v[196:199], v[126:129]
	v_mfma_f32_16x16x32_bf16 v[122:125], v[170:173], v[196:199], v[122:125]
	v_mfma_f32_16x16x32_bf16 v[110:113], v[162:165], v[204:207], v[110:113]
	v_mfma_f32_16x16x32_bf16 v[106:109], v[170:173], v[204:207], v[106:109]
	v_mfma_f32_16x16x32_bf16 v[94:97], v[162:165], v[212:215], v[94:97]
	v_mfma_f32_16x16x32_bf16 v[90:93], v[170:173], v[212:215], v[90:93]
	v_mfma_f32_16x16x32_bf16 v[78:81], v[162:165], v[220:223], v[78:81]
	v_mfma_f32_16x16x32_bf16 v[74:77], v[170:173], v[220:223], v[74:77]
	s_setprio 0
	s_setprio 1
	v_mfma_f32_16x16x32_bf16 v[118:121], v[174:177], v[192:195], v[118:121]
	v_mfma_f32_16x16x32_bf16 v[114:117], v[182:185], v[192:195], v[114:117]
	v_mfma_f32_16x16x32_bf16 v[102:105], v[174:177], v[200:203], v[102:105]
	v_mfma_f32_16x16x32_bf16 v[98:101], v[182:185], v[200:203], v[98:101]
	v_mfma_f32_16x16x32_bf16 v[86:89], v[174:177], v[208:211], v[86:89]
	v_mfma_f32_16x16x32_bf16 v[82:85], v[182:185], v[208:211], v[82:85]
	v_mfma_f32_16x16x32_bf16 v[70:73], v[174:177], v[216:219], v[70:73]
	v_mfma_f32_16x16x32_bf16 v[66:69], v[182:185], v[216:219], v[66:69]
	v_mfma_f32_16x16x32_bf16 v[118:121], v[178:181], v[196:199], v[118:121]
	v_mfma_f32_16x16x32_bf16 v[114:117], v[188:191], v[196:199], v[114:117]
	v_mfma_f32_16x16x32_bf16 v[102:105], v[178:181], v[204:207], v[102:105]
	v_mfma_f32_16x16x32_bf16 v[98:101], v[188:191], v[204:207], v[98:101]
	v_mfma_f32_16x16x32_bf16 v[86:89], v[178:181], v[212:215], v[86:89]
	v_mfma_f32_16x16x32_bf16 v[82:85], v[188:191], v[212:215], v[82:85]
	v_mfma_f32_16x16x32_bf16 v[70:73], v[178:181], v[220:223], v[70:73]
	v_mfma_f32_16x16x32_bf16 v[66:69], v[188:191], v[220:223], v[66:69]
	s_setprio 0
	s_barrier
	s_add_i32 s50, s38, s28
	v_lshl_add_u64 v[226:227], s[24:25], 0, v[130:131]
	s_mov_b32 m0, s50
	ds_read_b128 v[192:195], v152 offset:16384
	ds_read_b128 v[196:199], v152 offset:17408
	ds_read_b128 v[200:203], v152 offset:18432
	ds_read_b128 v[204:207], v152 offset:19456
	ds_read_b128 v[208:211], v152 offset:20480
	ds_read_b128 v[212:215], v152 offset:21504
	ds_read_b128 v[216:219], v152 offset:22528
	ds_read_b128 v[220:223], v152 offset:23552
	global_load_lds_dwordx4 v[226:227], off nt
	s_add_i32 m0, s50, 0x2000
	s_add_u32 s50, s24, 0x80000
	v_lshl_add_u64 v[228:229], s[24:25], 0, v[132:133]
	s_addc_u32 s51, s25, 0
	s_add_i32 s52, s39, s28
	global_load_lds_dwordx4 v[228:229], off nt
	v_lshl_add_u64 v[230:231], s[50:51], 0, v[130:131]
	s_mov_b32 m0, s52
	v_mov_b32_e32 v225, v135
	global_load_lds_dwordx4 v[230:231], off nt
	v_lshl_add_u64 v[230:231], s[50:51], 0, v[132:133]
	s_add_i32 m0, s52, 0x2000
	s_nop 0
	global_load_lds_dwordx4 v[230:231], off nt
	s_mov_b32 m0, s21
	v_lshl_add_u64 v[230:231], s[26:27], 0, v[134:135]
	global_load_lds_dwordx4 v134, s[26:27]
	s_mov_b32 m0, s31
	s_nop 0
	global_load_lds_dwordx4 v224, s[26:27]
	s_waitcnt vmcnt(8)
	s_waitcnt lgkmcnt(0)
	v_lshl_add_u64 v[224:225], s[26:27], 0, v[224:225]
	s_barrier
; #define PG8_STAGE(bufoff, gbase, voff) do { _Pragma("unroll") for (int _i = 0; _i < 2; ++_i) \
;         __builtin_amdgcn_global_load_lds((const unsigned*)((const char*)(gbase) + (voff)[_i]), (PG8_LAS unsigned*)(lds + (bufoff) + ldsw + _i * 8192), 16, 0, 0); } while (0)
; #define PG8_LDA(dst, b, h) do { _Pragma("unroll") for (int m = 0; m < 4; ++m) _Pragma("unroll") for (int k = 0; k < 2; ++k) dst[m][k] = *(const PG8_LAS bf16x8*)(lds + PG8_SA(b, h) + aoff + m * 2048 + k * 1024); } while (0)
; #define PG8_LDB(dst, b, h) do { _Pragma("unroll") for (int n = 0; n < 2; ++n) _Pragma("unroll") for (int k = 0; k < 2; ++k) dst[n][k] = *(const PG8_LAS bf16x8*)(lds + PG8_SB(b, h) + boff + n * 2048 + k * 1024); } while (0)
; #define PG8_MMA(ai, bj, At, Bt) do { __builtin_amdgcn_s_setprio(1); _Pragma("unroll") for (int m = 0; m < 4; ++m) _Pragma("unroll") for (int n = 0; n < 2; ++n) _Pragma("unroll") for (int k = 0; k < 2; ++k) \
;         acc[ai][bj][m][n] = __builtin_amdgcn_mfma_f32_16x16x32_bf16(Bt[n][k], At[m][k], acc[ai][bj][m][n], 0, 0, 0); __builtin_amdgcn_s_setprio(0); } while (0)
; #define PG8_WAIT_V(n) asm volatile("s_waitcnt vmcnt(" #n ")" ::: "memory")
; #define PG8_WAIT_L(n) asm volatile("s_waitcnt lgkmcnt(" #n ")" ::: "memory")
; #define PG8_BAR __builtin_amdgcn_s_barrier()
; #define PG8_SCHED __builtin_amdgcn_sched_barrier(0)
; #define PG8_STAGE(bufoff, gbase, voff) do { _Pragma("unroll") for (int _i = 0; _i < 2; ++_i) \
;         __builtin_amdgcn_global_load_lds((const unsigned*)((const char*)(gbase) + (voff)[_i]), (PG8_LAS unsigned*)(lds + (bufoff) + ldsw + _i * 8192), 16, 0, 0); } while (0)
; #define PG8_WAIT_V(n) asm volatile("s_waitcnt vmcnt(" #n ")" ::: "memory")
; #define PG8_WAIT_L(n) asm volatile("s_waitcnt lgkmcnt(" #n ")" ::: "memory")
; #define PG8_BAR __builtin_amdgcn_s_barrier()
; template <class Epi, class Sched>
; __device__ __forceinline__ void gemm_phase_gather(PG8_LAS unsigned char* lds, const Gemm g, const int* __restrict__ gidx, PG8_LAS int* itab  , const Sched& S, const Epi& E) {
;     ...
;             PG8_WAIT_V(8); PG8_WAIT_L(0); PG8_BAR; PG8_MMA(1, 0, At, B0); PG8_MMA(1, 1, At, B1); PG8_BAR; PG8_SCHED;
;             PG8_LDB(B0, 1, 0); PG8_LDB(B1, 1, 1); PG8_SCHED; PG8_LDA(At, 1, 0); PG8_STAGE(PG8_SA(0, 1), a2, vo2[1]);
;             PG8_WAIT_V(8); PG8_WAIT_L(0); PG8_BAR; PG8_MMA(0, 0, At, B0); PG8_MMA(0, 1, At, B1); PG8_BAR; PG8_SCHED;
	s_setprio 1
	s_waitcnt lgkmcnt(0)
	v_mfma_f32_16x16x32_bf16 v[62:65], v[158:161], v[192:195], v[62:65]
	v_mfma_f32_16x16x32_bf16 v[58:61], v[166:169], v[192:195], v[58:61]
	v_mfma_f32_16x16x32_bf16 v[46:49], v[158:161], v[200:203], v[46:49]
	v_mfma_f32_16x16x32_bf16 v[38:41], v[166:169], v[200:203], v[38:41]
	v_mfma_f32_16x16x32_bf16 v[14:17], v[158:161], v[208:211], v[14:17]
	v_mfma_f32_16x16x32_bf16 v[10:13], v[166:169], v[208:211], v[10:13]
	v_mfma_f32_16x16x32_bf16 v[6:9], v[158:161], v[216:219], v[6:9]
	v_mfma_f32_16x16x32_bf16 v[2:5], v[166:169], v[216:219], v[2:5]
	v_mfma_f32_16x16x32_bf16 v[62:65], v[162:165], v[196:199], v[62:65]
	v_mfma_f32_16x16x32_bf16 v[58:61], v[170:173], v[196:199], v[58:61]
	v_mfma_f32_16x16x32_bf16 v[46:49], v[162:165], v[204:207], v[46:49]
	v_mfma_f32_16x16x32_bf16 v[38:41], v[170:173], v[204:207], v[38:41]
	v_mfma_f32_16x16x32_bf16 v[14:17], v[162:165], v[212:215], v[14:17]
	v_mfma_f32_16x16x32_bf16 v[10:13], v[170:173], v[212:215], v[10:13]
	v_mfma_f32_16x16x32_bf16 v[6:9], v[162:165], v[220:223], v[6:9]
	v_mfma_f32_16x16x32_bf16 v[2:5], v[170:173], v[220:223], v[2:5]
	s_setprio 0
	s_setprio 1
	v_mfma_f32_16x16x32_bf16 v[54:57], v[174:177], v[192:195], v[54:57]
	v_mfma_f32_16x16x32_bf16 v[50:53], v[182:185], v[192:195], v[50:53]
	v_mfma_f32_16x16x32_bf16 v[30:33], v[174:177], v[200:203], v[30:33]
	v_mfma_f32_16x16x32_bf16 v[26:29], v[182:185], v[200:203], v[26:29]
	v_mfma_f32_16x16x32_bf16 v[42:45], v[174:177], v[208:211], v[42:45]
	v_mfma_f32_16x16x32_bf16 v[34:37], v[182:185], v[208:211], v[34:37]
	v_mfma_f32_16x16x32_bf16 v[22:25], v[174:177], v[216:219], v[22:25]
	v_mfma_f32_16x16x32_bf16 v[18:21], v[182:185], v[216:219], v[18:21]
	v_mfma_f32_16x16x32_bf16 v[54:57], v[178:181], v[196:199], v[54:57]
	v_mfma_f32_16x16x32_bf16 v[50:53], v[188:191], v[196:199], v[50:53]
	v_mfma_f32_16x16x32_bf16 v[30:33], v[178:181], v[204:207], v[30:33]
	v_mfma_f32_16x16x32_bf16 v[26:29], v[188:191], v[204:207], v[26:29]
	v_mfma_f32_16x16x32_bf16 v[42:45], v[178:181], v[212:215], v[42:45]
	v_mfma_f32_16x16x32_bf16 v[34:37], v[188:191], v[212:215], v[34:37]
	v_mfma_f32_16x16x32_bf16 v[22:25], v[178:181], v[220:223], v[22:25]
	v_mfma_f32_16x16x32_bf16 v[18:21], v[188:191], v[220:223], v[18:21]
	s_setprio 0
	s_barrier
	s_add_i32 s50, 0, 0x18000
	v_add_u32_e32 v134, s50, v148
	s_add_i32 s51, 0, 0x1c000
	ds_read_b128 v[158:161], v134
	ds_read_b128 v[162:165], v134 offset:1024
	ds_read_b128 v[166:169], v134 offset:2048
	ds_read_b128 v[170:173], v134 offset:3072
	v_add_u32_e32 v134, s51, v148
	ds_read_b128 v[174:177], v134
	ds_read_b128 v[178:181], v134 offset:1024
	ds_read_b128 v[182:185], v134 offset:2048
	ds_read_b128 v[188:191], v134 offset:3072
	s_mov_b32 m0, s33
	ds_read_b128 v[192:195], v152 offset:32768
	ds_read_b128 v[196:199], v152 offset:33792
	ds_read_b128 v[200:203], v152 offset:34816
	ds_read_b128 v[204:207], v152 offset:35840
	ds_read_b128 v[208:211], v152 offset:36864
	ds_read_b128 v[212:215], v152 offset:37888
	ds_read_b128 v[216:219], v152 offset:38912
	ds_read_b128 v[220:223], v152 offset:39936
	global_load_lds_dwordx4 v137, s[26:27]
	s_mov_b32 m0, s34
	s_nop 0
	global_load_lds_dwordx4 v139, s[26:27]
	s_waitcnt vmcnt(8)
	s_waitcnt lgkmcnt(0)
	s_barrier
	s_setprio 1
	s_waitcnt lgkmcnt(0)
	v_mfma_f32_16x16x32_bf16 v[126:129], v[158:161], v[192:195], v[126:129]
	v_mfma_f32_16x16x32_bf16 v[122:125], v[166:169], v[192:195], v[122:125]
	v_mfma_f32_16x16x32_bf16 v[110:113], v[158:161], v[200:203], v[110:113]
	v_mfma_f32_16x16x32_bf16 v[106:109], v[166:169], v[200:203], v[106:109]
	v_mfma_f32_16x16x32_bf16 v[94:97], v[158:161], v[208:211], v[94:97]
	v_mfma_f32_16x16x32_bf16 v[90:93], v[166:169], v[208:211], v[90:93]
	v_mfma_f32_16x16x32_bf16 v[78:81], v[158:161], v[216:219], v[78:81]
	v_mfma_f32_16x16x32_bf16 v[74:77], v[166:169], v[216:219], v[74:77]
	v_mfma_f32_16x16x32_bf16 v[126:129], v[162:165], v[196:199], v[126:129]
	v_mfma_f32_16x16x32_bf16 v[122:125], v[170:173], v[196:199], v[122:125]
	v_mfma_f32_16x16x32_bf16 v[110:113], v[162:165], v[204:207], v[110:113]
	v_mfma_f32_16x16x32_bf16 v[106:109], v[170:173], v[204:207], v[106:109]
	v_mfma_f32_16x16x32_bf16 v[94:97], v[162:165], v[212:215], v[94:97]
	v_mfma_f32_16x16x32_bf16 v[90:93], v[170:173], v[212:215], v[90:93]
	v_mfma_f32_16x16x32_bf16 v[78:81], v[162:165], v[220:223], v[78:81]
	v_mfma_f32_16x16x32_bf16 v[74:77], v[170:173], v[220:223], v[74:77]
	s_setprio 0
	s_setprio 1
	v_mfma_f32_16x16x32_bf16 v[118:121], v[174:177], v[192:195], v[118:121]
	v_mfma_f32_16x16x32_bf16 v[114:117], v[182:185], v[192:195], v[114:117]
	v_mfma_f32_16x16x32_bf16 v[102:105], v[174:177], v[200:203], v[102:105]
	v_mfma_f32_16x16x32_bf16 v[98:101], v[182:185], v[200:203], v[98:101]
	v_mfma_f32_16x16x32_bf16 v[86:89], v[174:177], v[208:211], v[86:89]
	v_mfma_f32_16x16x32_bf16 v[82:85], v[182:185], v[208:211], v[82:85]
	v_mfma_f32_16x16x32_bf16 v[70:73], v[174:177], v[216:219], v[70:73]
	v_mfma_f32_16x16x32_bf16 v[66:69], v[182:185], v[216:219], v[66:69]
	v_mfma_f32_16x16x32_bf16 v[118:121], v[178:181], v[196:199], v[118:121]
	v_mfma_f32_16x16x32_bf16 v[114:117], v[188:191], v[196:199], v[114:117]
	v_mfma_f32_16x16x32_bf16 v[102:105], v[178:181], v[204:207], v[102:105]
	v_mfma_f32_16x16x32_bf16 v[98:101], v[188:191], v[204:207], v[98:101]
	v_mfma_f32_16x16x32_bf16 v[86:89], v[178:181], v[212:215], v[86:89]
	v_mfma_f32_16x16x32_bf16 v[82:85], v[188:191], v[212:215], v[82:85]
	v_mfma_f32_16x16x32_bf16 v[70:73], v[178:181], v[220:223], v[70:73]
	v_mfma_f32_16x16x32_bf16 v[66:69], v[188:191], v[220:223], v[66:69]
	s_setprio 0
	s_barrier
; #define PG8_STAGE(bufoff, gbase, voff) do { _Pragma("unroll") for (int _i = 0; _i < 2; ++_i) \
;         __builtin_amdgcn_global_load_lds((const unsigned*)((const char*)(gbase) + (voff)[_i]), (PG8_LAS unsigned*)(lds + (bufoff) + ldsw + _i * 8192), 16, 0, 0); } while (0)
; #define PG8_LDA(dst, b, h) do { _Pragma("unroll") for (int m = 0; m < 4; ++m) _Pragma("unroll") for (int k = 0; k < 2; ++k) dst[m][k] = *(const PG8_LAS bf16x8*)(lds + PG8_SA(b, h) + aoff + m * 2048 + k * 1024); } while (0)
; #define PG8_MMA(ai, bj, At, Bt) do { __builtin_amdgcn_s_setprio(1); _Pragma("unroll") for (int m = 0; m < 4; ++m) _Pragma("unroll") for (int n = 0; n < 2; ++n) _Pragma("unroll") for (int k = 0; k < 2; ++k) \
;         acc[ai][bj][m][n] = __builtin_amdgcn_mfma_f32_16x16x32_bf16(Bt[n][k], At[m][k], acc[ai][bj][m][n], 0, 0, 0); __builtin_amdgcn_s_setprio(0); } while (0)
; #define PG8_WAIT_V(n) asm volatile("s_waitcnt vmcnt(" #n ")" ::: "memory")
; #define PG8_WAIT_L(n) asm volatile("s_waitcnt lgkmcnt(" #n ")" ::: "memory")
; #define PG8_BAR __builtin_amdgcn_s_barrier()
; #define PG8_SCHED __builtin_amdgcn_sched_barrier(0)
; #define PG8_STAGE(bufoff, gbase, voff) do { _Pragma("unroll") for (int _i = 0; _i < 2; ++_i) \
;         __builtin_amdgcn_global_load_lds((const unsigned*)((const char*)(gbase) + (voff)[_i]), (PG8_LAS unsigned*)(lds + (bufoff) + ldsw + _i * 8192), 16, 0, 0); } while (0)
; #define PG8_LDA(dst, b, h) do { _Pragma("unroll") for (int m = 0; m < 4; ++m) _Pragma("unroll") for (int k = 0; k < 2; ++k) dst[m][k] = *(const PG8_LAS bf16x8*)(lds + PG8_SA(b, h) + aoff + m * 2048 + k * 1024); } while (0)
; #define PG8_WAIT_V(n) asm volatile("s_waitcnt vmcnt(" #n ")" ::: "memory")
; #define PG8_WAIT_L(n) asm volatile("s_waitcnt lgkmcnt(" #n ")" ::: "memory")
; #define PG8_BAR __builtin_amdgcn_s_barrier()
; template <class Epi, class Sched>
; __device__ __forceinline__ void gemm_phase_gather(PG8_LAS unsigned char* lds, const Gemm g, const int* __restrict__ gidx, PG8_LAS int* itab  , const Sched& S, const Epi& E) {
;     ...
;             PG8_LDA(At, 1, 1); PG8_STAGE(PG8_SB(1, 0), b3, voffB); PG8_STAGE(PG8_SB(1, 1), b3 + hstep, voffB); PG8_STAGE(PG8_SA(1, 0), a3, vo2[0]);
;             PG8_WAIT_V(8); PG8_WAIT_L(0); PG8_BAR; PG8_MMA(1, 0, At, B0); PG8_MMA(1, 1, At, B1); PG8_BAR; PG8_SCHED;
;         }
;         if (wr == 0) PG8_BAR;
	s_add_i32 s26, s50, s28
	v_lshl_add_u64 v[226:227], v[226:227], 0, s[10:11]
	s_mov_b32 m0, s26
	ds_read_b128 v[192:195], v152 offset:49152
	ds_read_b128 v[196:199], v152 offset:50176
	ds_read_b128 v[200:203], v152 offset:51200
	ds_read_b128 v[204:207], v152 offset:52224
	ds_read_b128 v[208:211], v152 offset:53248
	ds_read_b128 v[212:215], v152 offset:54272
	ds_read_b128 v[216:219], v152 offset:55296
	ds_read_b128 v[220:223], v152 offset:56320
	global_load_lds_dwordx4 v[226:227], off nt
	s_add_i32 m0, s26, 0x2000
	s_add_u32 s24, s24, 0x80080
	v_lshl_add_u64 v[226:227], v[228:229], 0, s[10:11]
	s_addc_u32 s25, s25, 0
	s_add_i32 s26, s51, s28
	global_load_lds_dwordx4 v[226:227], off nt
	v_lshl_add_u64 v[226:227], s[24:25], 0, v[130:131]
	s_mov_b32 m0, s26
	v_lshl_add_u64 v[224:225], v[224:225], 0, s[10:11]
	global_load_lds_dwordx4 v[226:227], off nt
	v_lshl_add_u64 v[226:227], s[24:25], 0, v[132:133]
	s_add_i32 m0, s26, 0x2000
	s_nop 0
	global_load_lds_dwordx4 v[226:227], off nt
	v_lshl_add_u64 v[226:227], v[230:231], 0, s[10:11]
	s_mov_b32 m0, s35
	s_nop 0
	global_load_lds_dwordx4 v[226:227], off nt
	s_mov_b32 m0, s36
	s_nop 0
	global_load_lds_dwordx4 v[224:225], off nt
	s_waitcnt vmcnt(8)
	s_waitcnt lgkmcnt(0)
	s_barrier
	s_setprio 1
	s_waitcnt lgkmcnt(0)
	v_mfma_f32_16x16x32_bf16 v[62:65], v[158:161], v[192:195], v[62:65]
	v_mfma_f32_16x16x32_bf16 v[58:61], v[166:169], v[192:195], v[58:61]
	v_mfma_f32_16x16x32_bf16 v[46:49], v[158:161], v[200:203], v[46:49]
	v_mfma_f32_16x16x32_bf16 v[38:41], v[166:169], v[200:203], v[38:41]
	v_mfma_f32_16x16x32_bf16 v[14:17], v[158:161], v[208:211], v[14:17]
	v_mfma_f32_16x16x32_bf16 v[10:13], v[166:169], v[208:211], v[10:13]
	v_mfma_f32_16x16x32_bf16 v[6:9], v[158:161], v[216:219], v[6:9]
	v_mfma_f32_16x16x32_bf16 v[2:5], v[166:169], v[216:219], v[2:5]
	v_mfma_f32_16x16x32_bf16 v[62:65], v[162:165], v[196:199], v[62:65]
	v_mfma_f32_16x16x32_bf16 v[58:61], v[170:173], v[196:199], v[58:61]
	v_mfma_f32_16x16x32_bf16 v[46:49], v[162:165], v[204:207], v[46:49]
	v_mfma_f32_16x16x32_bf16 v[38:41], v[170:173], v[204:207], v[38:41]
	v_mfma_f32_16x16x32_bf16 v[14:17], v[162:165], v[212:215], v[14:17]
	v_mfma_f32_16x16x32_bf16 v[10:13], v[170:173], v[212:215], v[10:13]
	v_mfma_f32_16x16x32_bf16 v[6:9], v[162:165], v[220:223], v[6:9]
	v_mfma_f32_16x16x32_bf16 v[2:5], v[170:173], v[220:223], v[2:5]
	s_setprio 0
	s_setprio 1
	v_mfma_f32_16x16x32_bf16 v[54:57], v[174:177], v[192:195], v[54:57]
	v_mfma_f32_16x16x32_bf16 v[50:53], v[182:185], v[192:195], v[50:53]
	v_mfma_f32_16x16x32_bf16 v[30:33], v[174:177], v[200:203], v[30:33]
	v_mfma_f32_16x16x32_bf16 v[26:29], v[182:185], v[200:203], v[26:29]
	v_mfma_f32_16x16x32_bf16 v[42:45], v[174:177], v[208:211], v[42:45]
	v_mfma_f32_16x16x32_bf16 v[34:37], v[182:185], v[208:211], v[34:37]
	v_mfma_f32_16x16x32_bf16 v[22:25], v[174:177], v[216:219], v[22:25]
	v_mfma_f32_16x16x32_bf16 v[18:21], v[182:185], v[216:219], v[18:21]
	v_mfma_f32_16x16x32_bf16 v[54:57], v[178:181], v[196:199], v[54:57]
	v_mfma_f32_16x16x32_bf16 v[50:53], v[188:191], v[196:199], v[50:53]
	v_mfma_f32_16x16x32_bf16 v[30:33], v[178:181], v[204:207], v[30:33]
	v_mfma_f32_16x16x32_bf16 v[26:29], v[188:191], v[204:207], v[26:29]
	v_mfma_f32_16x16x32_bf16 v[42:45], v[178:181], v[212:215], v[42:45]
	v_mfma_f32_16x16x32_bf16 v[34:37], v[188:191], v[212:215], v[34:37]
	v_mfma_f32_16x16x32_bf16 v[22:25], v[178:181], v[220:223], v[22:25]
	v_mfma_f32_16x16x32_bf16 v[18:21], v[188:191], v[220:223], v[18:21]
	s_setprio 0
	s_barrier
	s_add_i32 s49, s49, 2
	s_add_u32 s22, s22, 0x100
	s_addc_u32 s23, s23, 0
	s_cmp_gt_u32 s49, 29
	s_cbranch_scc0 .LBB0_1278
	s_and_b64 vcc, exec, s[14:15]
	s_cbranch_vccz .LBB0_1281
	s_barrier
